# baseline (speedup 1.0000x reference)
.LBB6_9:
	v_lshlrev_b32_e32 v0, 5, v13
	v_or3_b32 v0, v0, s8, v14
	s_waitcnt vmcnt(0)
	s_nop 13
	v_accvgpr_read_b32 v21, a0
	v_accvgpr_read_b32 v20, a1
	v_accvgpr_read_b32 v19, a2
	v_accvgpr_read_b32 v18, a3
	v_accvgpr_read_b32 v17, a4
	v_accvgpr_read_b32 v16, a5
	v_accvgpr_read_b32 v15, a6
	v_accvgpr_read_b32 v10, a7
	v_accvgpr_read_b32 v9, a8
	v_accvgpr_read_b32 v8, a9
	v_accvgpr_read_b32 v7, a10
	v_accvgpr_read_b32 v6, a11
	v_accvgpr_read_b32 v5, a12
	v_accvgpr_read_b32 v4, a13
	v_accvgpr_read_b32 v3, a14
	v_accvgpr_read_b32 v2, a15
	v_cmp_gt_i32_e32 vcc, s20, v0
	s_and_saveexec_b64 s[2:3], vcc
	s_cbranch_execz .LBB6_11
	s_mul_i32 s2, s13, s4
	s_mul_hi_u32 s3, s12, s4
	s_add_i32 s3, s3, s2
	s_mul_i32 s2, s12, s4
	s_mul_i32 s8, s15, s4
	s_mul_hi_u32 s9, s14, s4
	s_add_i32 s9, s9, s8
	s_lshl_b64 s[2:3], s[2:3], 2
	s_waitcnt lgkmcnt(0)
	s_add_u32 s2, s10, s2
	v_ashrrev_i32_e32 v1, 31, v0
	s_addc_u32 s3, s11, s3
	v_lshlrev_b64 v[0:1], 2, v[0:1]
	v_lshl_add_u64 v[22:23], s[2:3], 0, v[0:1]
	global_load_dword v14, v[22:23], off
	s_load_dwordx2 s[0:1], s[0:1], 0x40
	s_mul_i32 s8, s14, s4
	v_lshl_add_u32 v11, v11, 5, s5
	s_lshl_b64 s[2:3], s[8:9], 2
	v_lshl_or_b32 v36, v12, 2, v11
	v_ashrrev_i32_e32 v11, 31, v11
	s_add_u32 s2, s6, s2
	v_or_b32_e32 v22, 1, v36
	v_or_b32_e32 v24, 2, v36
	v_or_b32_e32 v26, 3, v36
	v_or_b32_e32 v28, 8, v36
	v_or_b32_e32 v30, 9, v36
	v_or_b32_e32 v32, 10, v36
	v_or_b32_e32 v34, 11, v36
	s_waitcnt lgkmcnt(0)
	v_mul_lo_u32 v38, s0, v11
	v_mul_lo_u32 v11, s1, v36
	v_mad_u64_u32 v[12:13], s[4:5], s0, v36, 0
	s_addc_u32 s3, s7, s3
	v_mul_lo_u32 v39, s1, v22
	v_mad_u64_u32 v[22:23], s[4:5], s0, v22, 0
	v_mul_lo_u32 v40, s1, v24
	v_mad_u64_u32 v[24:25], s[4:5], s0, v24, 0
	v_mul_lo_u32 v41, s1, v26
	v_mad_u64_u32 v[26:27], s[4:5], s0, v26, 0
	v_mul_lo_u32 v42, s1, v28
	v_mad_u64_u32 v[28:29], s[4:5], s0, v28, 0
	v_mul_lo_u32 v43, s1, v30
	v_mad_u64_u32 v[30:31], s[4:5], s0, v30, 0
	v_mul_lo_u32 v44, s1, v32
	v_mad_u64_u32 v[32:33], s[4:5], s0, v32, 0
	v_mul_lo_u32 v45, s1, v34
	v_mad_u64_u32 v[34:35], s[4:5], s0, v34, 0
	v_add3_u32 v13, v13, v38, v11
	v_lshl_add_u64 v[0:1], s[2:3], 0, v[0:1]
	v_or_b32_e32 v37, 16, v36
	v_add3_u32 v23, v23, v38, v39
	v_add3_u32 v25, v25, v38, v40
	v_add3_u32 v27, v27, v38, v41
	v_add3_u32 v29, v29, v38, v42
	v_add3_u32 v31, v31, v38, v43
	v_add3_u32 v33, v33, v38, v44
	v_add3_u32 v35, v35, v38, v45
	v_lshl_add_u64 v[12:13], v[12:13], 2, v[0:1]
	v_lshl_add_u64 v[22:23], v[22:23], 2, v[0:1]
	v_lshl_add_u64 v[24:25], v[24:25], 2, v[0:1]
	v_lshl_add_u64 v[26:27], v[26:27], 2, v[0:1]
	v_lshl_add_u64 v[28:29], v[28:29], 2, v[0:1]
	v_lshl_add_u64 v[30:31], v[30:31], 2, v[0:1]
	v_lshl_add_u64 v[32:33], v[32:33], 2, v[0:1]
	v_lshl_add_u64 v[34:35], v[34:35], 2, v[0:1]
	s_waitcnt vmcnt(0)
	v_add_f32_e32 v11, v14, v21
	v_add_f32_e32 v10, v14, v10
	v_add_f32_e32 v20, v14, v20
	v_add_f32_e32 v19, v14, v19
	v_add_f32_e32 v18, v14, v18
	v_add_f32_e32 v17, v14, v17
	v_add_f32_e32 v16, v14, v16
	v_add_f32_e32 v15, v14, v15
	global_store_dword v[12:13], v11, off sc1
	global_store_dword v[22:23], v20, off sc1
	global_store_dword v[24:25], v19, off sc1
	global_store_dword v[26:27], v18, off sc1
	global_store_dword v[28:29], v17, off sc1
	global_store_dword v[30:31], v16, off sc1
	global_store_dword v[32:33], v15, off sc1
	global_store_dword v[34:35], v10, off sc1
	v_mul_lo_u32 v12, s1, v37
	v_mad_u64_u32 v[10:11], s[2:3], s0, v37, 0
	v_add3_u32 v11, v11, v38, v12
	v_add_f32_e32 v9, v14, v9
	v_lshl_add_u64 v[10:11], v[10:11], 2, v[0:1]
	global_store_dword v[10:11], v9, off sc1
	v_or_b32_e32 v9, 17, v36
	v_add_f32_e32 v10, v14, v8
	v_mul_lo_u32 v11, s1, v9
	v_mad_u64_u32 v[8:9], s[2:3], s0, v9, 0
	v_add3_u32 v9, v9, v38, v11
	v_lshl_add_u64 v[8:9], v[8:9], 2, v[0:1]
	global_store_dword v[8:9], v10, off sc1
	v_or_b32_e32 v8, 18, v36
	v_mul_lo_u32 v10, s1, v8
	v_mad_u64_u32 v[8:9], s[2:3], s0, v8, 0
	v_add3_u32 v9, v9, v38, v10
	v_add_f32_e32 v7, v14, v7
	v_lshl_add_u64 v[8:9], v[8:9], 2, v[0:1]
	global_store_dword v[8:9], v7, off sc1
	v_or_b32_e32 v7, 19, v36
	v_add_f32_e32 v8, v14, v6
	v_mul_lo_u32 v9, s1, v7
	v_mad_u64_u32 v[6:7], s[2:3], s0, v7, 0
	v_add3_u32 v7, v7, v38, v9
	v_lshl_add_u64 v[6:7], v[6:7], 2, v[0:1]
	global_store_dword v[6:7], v8, off sc1
	v_or_b32_e32 v6, 24, v36
	v_mul_lo_u32 v8, s1, v6
	v_mad_u64_u32 v[6:7], s[2:3], s0, v6, 0
	v_add3_u32 v7, v7, v38, v8
	v_add_f32_e32 v5, v14, v5
	v_lshl_add_u64 v[6:7], v[6:7], 2, v[0:1]
	global_store_dword v[6:7], v5, off sc1
	v_or_b32_e32 v5, 25, v36
	v_add_f32_e32 v6, v14, v4
	v_mul_lo_u32 v7, s1, v5
	v_mad_u64_u32 v[4:5], s[2:3], s0, v5, 0
	v_add3_u32 v5, v5, v38, v7
	v_lshl_add_u64 v[4:5], v[4:5], 2, v[0:1]
	global_store_dword v[4:5], v6, off sc1
	v_or_b32_e32 v4, 26, v36
	v_mul_lo_u32 v6, s1, v4
	v_mad_u64_u32 v[4:5], s[2:3], s0, v4, 0
	v_add3_u32 v5, v5, v38, v6
	v_add_f32_e32 v3, v14, v3
	v_lshl_add_u64 v[4:5], v[4:5], 2, v[0:1]
	global_store_dword v[4:5], v3, off sc1
	v_or_b32_e32 v3, 27, v36
	v_add_f32_e32 v4, v14, v2
	v_mul_lo_u32 v5, s1, v3
	v_mad_u64_u32 v[2:3], s[0:1], s0, v3, 0
	v_add3_u32 v3, v3, v38, v5
	v_lshl_add_u64 v[0:1], v[2:3], 2, v[0:1]
	global_store_dword v[0:1], v4, off sc1
